# baseline (speedup 1.0000x reference)
_Z13logits_kernelPKDv8_DF16bS1_PKfS3_PDv2_fS5_Pf:
	s_load_dwordx4 s[4:7], s[0:1], 0x0
	s_load_dwordx4 s[12:15], s[0:1], 0x10
	s_load_dwordx4 s[24:27], s[0:1], 0x20
	s_load_dwordx2 s[28:29], s[0:1], 0x30
	s_lshl_b32 s3, s2, 1
	s_and_b32 s3, s3, 14
	s_ashr_i32 s8, s2, 7
	s_bfe_u32 s10, s2, 0x40003
	s_add_i32 s3, s3, s8
	v_lshrrev_b32_e32 v1, 6, v0
	v_and_b32_e32 v2, 63, v0
	s_movk_i32 s11, 0x3000
	v_lshlrev_b32_e32 v2, 4, v2
	v_and_b32_e32 v5, 31, v0
	v_mad_u32_u24 v2, v1, s11, v2
	v_lshlrev_b32_e32 v5, 2, v5
	s_lshl_b32 s9, s3, 9
	v_add_u32_e32 v3, 0x1000, v2
	v_add_u32_e32 v4, 0x2000, v2
	v_add_u32_e32 v5, s9, v5
	s_mul_i32 s8, s10, 0xc000
	s_mul_i32 s9, s3, 0x30000
	s_waitcnt lgkmcnt(0)
	s_load_dword s22, s[14:15], 0x0
	global_load_dword v248, v5, s[12:13]
	global_load_dword v249, v5, s[12:13] offset:128
	global_load_dword v250, v5, s[12:13] offset:256
	global_load_dword v251, v5, s[12:13] offset:384
	s_add_u32 s4, s4, s8
	s_addc_u32 s5, s5, 0
	s_add_u32 s6, s6, s9
	s_addc_u32 s7, s7, 0
	s_add_u32 s16, s6, 0xc000
	s_addc_u32 s17, s7, 0
	s_add_u32 s18, s6, 0x18000
	s_addc_u32 s19, s7, 0
	s_add_u32 s20, s6, 0x24000
	s_addc_u32 s21, s7, 0
	global_load_dwordx4 v[8:11], v2, s[4:5]
	global_load_dwordx4 v[56:59], v2, s[6:7]
	global_load_dwordx4 v[104:107], v2, s[16:17]
	global_load_dwordx4 v[152:155], v2, s[18:19]
	global_load_dwordx4 v[200:203], v2, s[20:21]
	global_load_dwordx4 v[12:15], v2, s[4:5] offset:1024
	global_load_dwordx4 v[60:63], v2, s[6:7] offset:1024
	global_load_dwordx4 v[108:111], v2, s[16:17] offset:1024
	global_load_dwordx4 v[156:159], v2, s[18:19] offset:1024
	global_load_dwordx4 v[204:207], v2, s[20:21] offset:1024
	global_load_dwordx4 v[16:19], v2, s[4:5] offset:2048
	global_load_dwordx4 v[64:67], v2, s[6:7] offset:2048
	global_load_dwordx4 v[112:115], v2, s[16:17] offset:2048
	global_load_dwordx4 v[160:163], v2, s[18:19] offset:2048
	global_load_dwordx4 v[208:211], v2, s[20:21] offset:2048
	global_load_dwordx4 v[20:23], v2, s[4:5] offset:3072
	global_load_dwordx4 v[68:71], v2, s[6:7] offset:3072
	global_load_dwordx4 v[116:119], v2, s[16:17] offset:3072
	global_load_dwordx4 v[164:167], v2, s[18:19] offset:3072
	global_load_dwordx4 v[212:215], v2, s[20:21] offset:3072
	global_load_dwordx4 v[24:27], v3, s[4:5]
	global_load_dwordx4 v[72:75], v3, s[6:7]
	global_load_dwordx4 v[120:123], v3, s[16:17]
	global_load_dwordx4 v[168:171], v3, s[18:19]
	global_load_dwordx4 v[216:219], v3, s[20:21]
	global_load_dwordx4 v[28:31], v3, s[4:5] offset:1024
	global_load_dwordx4 v[76:79], v3, s[6:7] offset:1024
	global_load_dwordx4 v[124:127], v3, s[16:17] offset:1024
	global_load_dwordx4 v[172:175], v3, s[18:19] offset:1024
	global_load_dwordx4 v[220:223], v3, s[20:21] offset:1024
	global_load_dwordx4 v[32:35], v3, s[4:5] offset:2048
	global_load_dwordx4 v[80:83], v3, s[6:7] offset:2048
	global_load_dwordx4 v[128:131], v3, s[16:17] offset:2048
	global_load_dwordx4 v[176:179], v3, s[18:19] offset:2048
	global_load_dwordx4 v[224:227], v3, s[20:21] offset:2048
	global_load_dwordx4 v[36:39], v3, s[4:5] offset:3072
	global_load_dwordx4 v[84:87], v3, s[6:7] offset:3072
	global_load_dwordx4 v[132:135], v3, s[16:17] offset:3072
	global_load_dwordx4 v[180:183], v3, s[18:19] offset:3072
	global_load_dwordx4 v[228:231], v3, s[20:21] offset:3072
	global_load_dwordx4 v[40:43], v4, s[4:5]
	global_load_dwordx4 v[88:91], v4, s[6:7]
	global_load_dwordx4 v[136:139], v4, s[16:17]
	global_load_dwordx4 v[184:187], v4, s[18:19]
	global_load_dwordx4 v[232:235], v4, s[20:21]
	global_load_dwordx4 v[44:47], v4, s[4:5] offset:1024
	global_load_dwordx4 v[92:95], v4, s[6:7] offset:1024
	global_load_dwordx4 v[140:143], v4, s[16:17] offset:1024
	global_load_dwordx4 v[188:191], v4, s[18:19] offset:1024
	global_load_dwordx4 v[236:239], v4, s[20:21] offset:1024
	global_load_dwordx4 v[48:51], v4, s[4:5] offset:2048
	global_load_dwordx4 v[96:99], v4, s[6:7] offset:2048
	global_load_dwordx4 v[144:147], v4, s[16:17] offset:2048
	global_load_dwordx4 v[192:195], v4, s[18:19] offset:2048
	global_load_dwordx4 v[240:243], v4, s[20:21] offset:2048
	global_load_dwordx4 v[52:55], v4, s[4:5] offset:3072
	global_load_dwordx4 v[100:103], v4, s[6:7] offset:3072
	global_load_dwordx4 v[148:151], v4, s[16:17] offset:3072
	global_load_dwordx4 v[196:199], v4, s[18:19] offset:3072
	global_load_dwordx4 v[244:247], v4, s[20:21] offset:3072
	s_waitcnt vmcnt(58)
	v_mfma_f32_32x32x16_bf16 a[0:15], v[8:11], v[56:59], 0
	s_waitcnt vmcnt(57)
	v_mfma_f32_32x32x16_bf16 a[0:15], v[8:11], v[104:107], a[0:15]
	s_waitcnt vmcnt(56)
	v_mfma_f32_32x32x16_bf16 a[0:15], v[8:11], v[152:155], a[0:15]
	s_waitcnt vmcnt(55)
	v_mfma_f32_32x32x16_bf16 a[0:15], v[8:11], v[200:203], a[0:15]
	s_waitcnt vmcnt(53)
	v_mfma_f32_32x32x16_bf16 a[0:15], v[12:15], v[60:63], a[0:15]
	s_waitcnt vmcnt(52)
	v_mfma_f32_32x32x16_bf16 a[0:15], v[12:15], v[108:111], a[0:15]
	s_waitcnt vmcnt(51)
	v_mfma_f32_32x32x16_bf16 a[0:15], v[12:15], v[156:159], a[0:15]
	s_waitcnt vmcnt(50)
	v_mfma_f32_32x32x16_bf16 a[0:15], v[12:15], v[204:207], a[0:15]
	s_waitcnt vmcnt(48)
	v_mfma_f32_32x32x16_bf16 a[0:15], v[16:19], v[64:67], a[0:15]
	s_waitcnt vmcnt(47)
	v_mfma_f32_32x32x16_bf16 a[0:15], v[16:19], v[112:115], a[0:15]
	s_waitcnt vmcnt(46)
	v_mfma_f32_32x32x16_bf16 a[0:15], v[16:19], v[160:163], a[0:15]
	s_waitcnt vmcnt(45)
	v_mfma_f32_32x32x16_bf16 a[0:15], v[16:19], v[208:211], a[0:15]
	s_waitcnt vmcnt(43)
	v_mfma_f32_32x32x16_bf16 a[0:15], v[20:23], v[68:71], a[0:15]
	s_waitcnt vmcnt(42)
	v_mfma_f32_32x32x16_bf16 a[0:15], v[20:23], v[116:119], a[0:15]
	s_waitcnt vmcnt(41)
	v_mfma_f32_32x32x16_bf16 a[0:15], v[20:23], v[164:167], a[0:15]
	s_waitcnt vmcnt(40)
	v_mfma_f32_32x32x16_bf16 a[0:15], v[20:23], v[212:215], a[0:15]
	s_waitcnt vmcnt(38)
	v_mfma_f32_32x32x16_bf16 a[0:15], v[24:27], v[72:75], a[0:15]
	s_waitcnt vmcnt(37)
	v_mfma_f32_32x32x16_bf16 a[0:15], v[24:27], v[120:123], a[0:15]
	s_waitcnt vmcnt(36)
	v_mfma_f32_32x32x16_bf16 a[0:15], v[24:27], v[168:171], a[0:15]
	s_waitcnt vmcnt(35)
	v_mfma_f32_32x32x16_bf16 a[0:15], v[24:27], v[216:219], a[0:15]
	s_waitcnt vmcnt(33)
	v_mfma_f32_32x32x16_bf16 a[0:15], v[28:31], v[76:79], a[0:15]
	s_waitcnt vmcnt(32)
	v_mfma_f32_32x32x16_bf16 a[0:15], v[28:31], v[124:127], a[0:15]
	s_waitcnt vmcnt(31)
	v_mfma_f32_32x32x16_bf16 a[0:15], v[28:31], v[172:175], a[0:15]
	s_waitcnt vmcnt(30)
	v_mfma_f32_32x32x16_bf16 a[0:15], v[28:31], v[220:223], a[0:15]
	s_waitcnt vmcnt(28)
	v_mfma_f32_32x32x16_bf16 a[0:15], v[32:35], v[80:83], a[0:15]
	s_waitcnt vmcnt(27)
	v_mfma_f32_32x32x16_bf16 a[0:15], v[32:35], v[128:131], a[0:15]
	s_waitcnt vmcnt(26)
	v_mfma_f32_32x32x16_bf16 a[0:15], v[32:35], v[176:179], a[0:15]
	s_waitcnt vmcnt(25)
	v_mfma_f32_32x32x16_bf16 a[0:15], v[32:35], v[224:227], a[0:15]
	s_waitcnt vmcnt(23)
	v_mfma_f32_32x32x16_bf16 a[0:15], v[36:39], v[84:87], a[0:15]
	s_waitcnt vmcnt(22)
	v_mfma_f32_32x32x16_bf16 a[0:15], v[36:39], v[132:135], a[0:15]
	s_waitcnt vmcnt(21)
	v_mfma_f32_32x32x16_bf16 a[0:15], v[36:39], v[180:183], a[0:15]
	s_waitcnt vmcnt(20)
	v_mfma_f32_32x32x16_bf16 a[0:15], v[36:39], v[228:231], a[0:15]
	s_waitcnt vmcnt(18)
	v_mfma_f32_32x32x16_bf16 a[0:15], v[40:43], v[88:91], a[0:15]
	s_waitcnt vmcnt(17)
	v_mfma_f32_32x32x16_bf16 a[0:15], v[40:43], v[136:139], a[0:15]
	s_waitcnt vmcnt(16)
	v_mfma_f32_32x32x16_bf16 a[0:15], v[40:43], v[184:187], a[0:15]
	s_waitcnt vmcnt(15)
	v_mfma_f32_32x32x16_bf16 a[0:15], v[40:43], v[232:235], a[0:15]
	s_waitcnt vmcnt(13)
	v_mfma_f32_32x32x16_bf16 a[0:15], v[44:47], v[92:95], a[0:15]
	s_waitcnt vmcnt(12)
	v_mfma_f32_32x32x16_bf16 a[0:15], v[44:47], v[140:143], a[0:15]
	s_waitcnt vmcnt(11)
	v_mfma_f32_32x32x16_bf16 a[0:15], v[44:47], v[188:191], a[0:15]
	s_waitcnt vmcnt(10)
	v_mfma_f32_32x32x16_bf16 a[0:15], v[44:47], v[236:239], a[0:15]
	v_add_f32_e32 v8, 0, v248
	v_add_f32_e32 v8, v8, v249
	v_add_f32_e32 v8, v8, v250
	v_add_f32_e32 v8, v8, v251
	v_mov_b32_e32 v9, 0x3fb8aa3b
	s_waitcnt lgkmcnt(0)
	v_mul_f32_e32 v9, s22, v9
	v_exp_f32_e32 v9, v9
	v_add_f32_e32 v10, 0x2b8cbccc, v8
	v_div_scale_f32 v11, s[8:9], v10, v10, v9
	v_rcp_f32_e32 v12, v11
	v_div_scale_f32 v13, vcc, v9, v10, v9
	v_fma_f32 v14, -v11, v12, 1.0
	v_fmac_f32_e32 v12, v14, v12
	v_mul_f32_e32 v14, v13, v12
	v_fma_f32 v15, -v11, v14, v13
	v_fmac_f32_e32 v14, v15, v12
	v_fma_f32 v11, -v11, v14, v13
	v_div_fmas_f32 v11, v11, v12, v14
	v_div_fixup_f32 v9, v11, v10, v9
	v_lshlrev_b32_e32 v10, 2, v0
	v_add_u32_e32 v10, 0x4000, v10
	v_cmp_gt_u32_e32 vcc, 32, v0
	s_and_saveexec_b64 s[8:9], vcc
	ds_write2_b32 v10, v8, v9 offset0:128 offset1:160
	s_mov_b64 exec, s[8:9]
	s_waitcnt vmcnt(8)
	v_mfma_f32_32x32x16_bf16 a[0:15], v[48:51], v[96:99], a[0:15]
	s_waitcnt vmcnt(7)
	v_mfma_f32_32x32x16_bf16 a[0:15], v[48:51], v[144:147], a[0:15]
	s_waitcnt vmcnt(6)
	v_mfma_f32_32x32x16_bf16 a[0:15], v[48:51], v[192:195], a[0:15]
	s_waitcnt vmcnt(5)
	v_mfma_f32_32x32x16_bf16 a[0:15], v[48:51], v[240:243], a[0:15]
	v_mul_u32_u24_e32 v1, 0x1080, v1
	s_movk_i32 s4, 0x7f
	s_movk_i32 s6, 0x84
	v_cmp_lt_u32_e32 vcc, s4, v0
	v_lshrrev_b32_e32 v11, 3, v0
	v_and_b32_e32 v10, 31, v0
	v_and_b32_e32 v11, 4, v11
	v_mul_u32_u24_e32 v11, 0x84, v11
	v_lshlrev_b32_e32 v9, 2, v10
	v_bfe_u32 v6, v0, 2, 5
	v_and_b32_e32 v7, 3, v0
	v_add3_u32 v1, v1, v11, v9
	v_lshlrev_b32_e32 v8, 3, v7
	s_waitcnt vmcnt(3)
	v_mfma_f32_32x32x16_bf16 a[0:15], v[52:55], v[100:103], a[0:15]
	s_waitcnt vmcnt(2)
	v_mfma_f32_32x32x16_bf16 a[0:15], v[52:55], v[148:151], a[0:15]
	s_waitcnt vmcnt(1)
	v_mfma_f32_32x32x16_bf16 a[0:15], v[52:55], v[196:199], a[0:15]
	s_waitcnt vmcnt(0)
	v_mfma_f32_32x32x16_bf16 a[0:15], v[52:55], v[244:247], a[0:15]
	s_nop 11
	ds_write_b32 v1, a0
	ds_write_b32 v1, a1 offset:132
	ds_write_b32 v1, a2 offset:264
	ds_write_b32 v1, a3 offset:396
	ds_write_b32 v1, a4 offset:1056
	ds_write_b32 v1, a5 offset:1188
	ds_write_b32 v1, a6 offset:1320
	ds_write_b32 v1, a7 offset:1452
	ds_write_b32 v1, a8 offset:2112
	ds_write_b32 v1, a9 offset:2244
	ds_write_b32 v1, a10 offset:2376
	ds_write_b32 v1, a11 offset:2508
	ds_write_b32 v1, a12 offset:3168
	ds_write_b32 v1, a13 offset:3300
	ds_write_b32 v1, a14 offset:3432
	ds_write_b32 v1, a15 offset:3564
	v_bfe_u32 v6, v0, 2, 5
	v_and_b32_e32 v7, 3, v0
	v_lshlrev_b32_e32 v9, 3, v7
	v_readfirstlane_b32 s30, v0
	v_sub_u32_e32 v10, v6, v9
	s_waitcnt lgkmcnt(0)
	s_barrier
	s_cmpk_ge_u32 s30, 0x80
	s_cbranch_scc1 .Llg_k1
	v_mul_u32_u24_e32 v2, 0x84, v6
	v_lshlrev_b32_e32 v8, 5, v7
	v_add_u32_e32 v2, v2, v8
	v_add_u32_e32 v8, 0x4280, v8
	v_add_u32_e32 v3, 0x1080, v2
	v_add_u32_e32 v4, 0x2100, v2
	v_add_u32_e32 v5, 0x3180, v2
	ds_read_b128 v[48:51], v8
	ds_read_b128 v[52:55], v8 offset:16
	ds_read2_b32 v[16:17], v2 offset0:0 offset1:1
	ds_read2_b32 v[18:19], v2 offset0:2 offset1:3
	ds_read2_b32 v[20:21], v2 offset0:4 offset1:5
	ds_read2_b32 v[22:23], v2 offset0:6 offset1:7
	ds_read2_b32 v[24:25], v3 offset0:0 offset1:1
	ds_read2_b32 v[26:27], v3 offset0:2 offset1:3
	ds_read2_b32 v[28:29], v3 offset0:4 offset1:5
	ds_read2_b32 v[30:31], v3 offset0:6 offset1:7
	ds_read2_b32 v[32:33], v4 offset0:0 offset1:1
	ds_read2_b32 v[34:35], v4 offset0:2 offset1:3
	ds_read2_b32 v[36:37], v4 offset0:4 offset1:5
	ds_read2_b32 v[38:39], v4 offset0:6 offset1:7
	s_waitcnt lgkmcnt(4)
	ds_read2_b32 v[40:41], v5 offset0:0 offset1:1
	ds_read2_b32 v[42:43], v5 offset0:2 offset1:3
	ds_read2_b32 v[44:45], v5 offset0:4 offset1:5
	ds_read2_b32 v[46:47], v5 offset0:6 offset1:7
	s_waitcnt lgkmcnt(0)
	s_branch .Llg_join
